# GLA chunk-state store (G1): half-waves exchange 8-byte pieces with v_permlane32_swap, 8 global_store_dwordx4 instead of 16 global_store_dwordx2 per wave and item
# speedup vs baseline: 1.0025x; 1.0025x over previous
; #define FA_SBAR() __builtin_amdgcn_sched_barrier(0)
; __device__ __forceinline__ int v_rd_base(int lane) { return ((lane & 3) << 3) | (((lane >> 2) & 3) << 6) | (((lane >> 4) & 1) << 5) | (((lane >> 5) & 1) << 8); }
; __device__ __forceinline__ fa::s16x4 tr_read_dyn(int addr) { fa::s16x4 r; asm volatile("ds_read_b64_tr_b16 %0, %1" : "=&v"(r) : "v"(addr) : "memory"); return r; }
; __device__ __forceinline__ void gla_g1(LAS unsigned char* lds, const bf16* Z, bf16* ST, float* DEC, const GlaPre pre, const float (&wa)[16], const float ba, int item, int tid) {
;     ...
;     const int rb = v_rd_base(lane); const int vbV = (int)(uintptr_t)(lds + GL_V) + (wid >> 2) * 16384 + rb, vbK = (int)(uintptr_t)(lds + GL_KS) + rb;
; #pragma unroll
;     for (int ks = 0; ks < 4; ++ks) {
;         s16x4 bl = tr_read_dyn(vbV + v_rd_off(wid & 3, ks, 0)), bhh = tr_read_dyn(vbV + v_rd_off(wid & 3, ks, 1));
;         s16x4 al[4], ah[4];
; #pragma unroll
;         for (int kt = 0; kt < 4; ++kt) { al[kt] = tr_read_dyn(vbK + v_rd_off(kt, ks, 0)); ah[kt] = tr_read_dyn(vbK + v_rd_off(kt, ks, 1)); }
;         asm volatile("s_waitcnt lgkmcnt(0)" : "+v"(bl), "+v"(bhh), "+v"(al[0]), "+v"(ah[0]), "+v"(al[1]), "+v"(ah[1]), "+v"(al[2]), "+v"(ah[2]), "+v"(al[3]), "+v"(ah[3]) :: "memory"); FA_SBAR();
; #pragma unroll
;         for (int kt = 0; kt < 4; ++kt) acc[kt] = __builtin_amdgcn_mfma_f32_32x32x16_bf16(GL_PK(al[kt], ah[kt]), GL_PK(bl, bhh), acc[kt], 0, 0, 0);
;     }
.LBB0_915:
	s_or_b64 exec, exec, s[14:15]
	s_lshl_b32 s15, s18, 6
	v_and_b32_e32 v2, 0xc0, v39
	v_lshlrev_b32_e32 v3, 1, v70
	s_and_b32 s15, s15, 0xffffc000
	v_and_or_b32 v2, v50, 24, v2
	v_and_b32_e32 v3, 32, v3
	v_and_b32_e32 v4, 0x100, v50
	s_add_i32 s15, s15, 0
	v_or3_b32 v69, v2, v3, v4
	s_add_i32 s15, s15, 0x10000
	s_ashr_i32 s14, s18, 6
	v_add_u32_e32 v71, s15, v69
	s_add_i32 s15, 0, 0x8000
	v_add_u32_e32 v8, s15, v69
	s_lshl_b32 s15, s14, 9
	s_and_b32 s15, s15, 0x600
	s_waitcnt lgkmcnt(0)
	s_barrier
	v_add_u32_e32 v94, 0x800, v71
	v_add_u32_e32 v4, s15, v71
	ds_read_b64_tr_b16 v[2:3], v4
	v_add_u32_e32 v6, s15, v94
	ds_read_b64_tr_b16 v[4:5], v6
	v_readlane_b32 s16, v254, 46
	ds_read_b64_tr_b16 v[6:7], v8
	v_and_b32_e32 v0, 31, v70
	s_nop 0
	v_add_u32_e32 v10, s16, v69
	ds_read_b64_tr_b16 v[8:9], v10
	v_readlane_b32 s16, v254, 47
	s_nop 1
	v_add_u32_e32 v12, s16, v69
	ds_read_b64_tr_b16 v[10:11], v12
	v_readlane_b32 s16, v254, 48
	s_nop 1
	v_add_u32_e32 v14, s16, v69
	ds_read_b64_tr_b16 v[12:13], v14
	v_readlane_b32 s16, v254, 49
	s_nop 1
	v_add_u32_e32 v16, s16, v69
	ds_read_b64_tr_b16 v[14:15], v16
	v_readlane_b32 s16, v254, 50
	s_nop 1
	v_add_u32_e32 v18, s16, v69
	ds_read_b64_tr_b16 v[16:17], v18
	v_readlane_b32 s16, v254, 51
	s_nop 1
	v_add_u32_e32 v18, s16, v69
	ds_read_b64_tr_b16 v[74:75], v18
	v_readlane_b32 s16, v254, 52
	s_nop 1
	v_add_u32_e32 v18, s16, v69
	ds_read_b64_tr_b16 v[76:77], v18
	s_nop 0
	s_waitcnt lgkmcnt(0)
	s_or_b32 s16, s15, 0x1000
	v_mfma_f32_32x32x16_bf16 v[50:65], v[6:9], v[2:5], 0
	v_add_u32_e32 v78, s16, v94
	v_mfma_f32_32x32x16_bf16 v[34:49], v[10:13], v[2:5], 0
	v_mfma_f32_32x32x16_bf16 v[18:33], v[14:17], v[2:5], 0
	v_mfma_f32_32x32x16_bf16 v[2:17], v[74:77], v[2:5], 0
	v_add_u32_e32 v76, s16, v71
	ds_read_b64_tr_b16 v[74:75], v76
	ds_read_b64_tr_b16 v[76:77], v78
	v_readlane_b32 s16, v254, 53
	s_nop 1
	v_add_u32_e32 v80, s16, v69
	ds_read_b64_tr_b16 v[78:79], v80
	v_readlane_b32 s16, v254, 54
	s_nop 1
	v_add_u32_e32 v82, s16, v69
	ds_read_b64_tr_b16 v[80:81], v82
	v_readlane_b32 s16, v254, 55
	s_nop 1
	v_add_u32_e32 v84, s16, v69
	ds_read_b64_tr_b16 v[82:83], v84
	v_readlane_b32 s16, v254, 56
	s_nop 1
	v_add_u32_e32 v86, s16, v69
	ds_read_b64_tr_b16 v[84:85], v86
	v_readlane_b32 s16, v254, 57
	s_nop 1
	v_add_u32_e32 v88, s16, v69
	ds_read_b64_tr_b16 v[86:87], v88
	v_readlane_b32 s16, v254, 58
	s_nop 1
	v_add_u32_e32 v90, s16, v69
	ds_read_b64_tr_b16 v[88:89], v90
	v_readlane_b32 s16, v254, 59
	s_nop 1
	v_add_u32_e32 v92, s16, v69
	ds_read_b64_tr_b16 v[90:91], v92
	v_readlane_b32 s16, v254, 60
	s_nop 1
	v_add_u32_e32 v95, s16, v69
	ds_read_b64_tr_b16 v[92:93], v95
	s_nop 0
	s_waitcnt lgkmcnt(0)
	s_or_b32 s16, s15, 0x2000
	v_mfma_f32_32x32x16_bf16 v[50:65], v[78:81], v[74:77], v[50:65]
	v_add_u32_e32 v78, s16, v94
	v_mfma_f32_32x32x16_bf16 v[34:49], v[82:85], v[74:77], v[34:49]
	v_mfma_f32_32x32x16_bf16 v[18:33], v[86:89], v[74:77], v[18:33]
	v_mfma_f32_32x32x16_bf16 v[2:17], v[90:93], v[74:77], v[2:17]
	v_add_u32_e32 v76, s16, v71
	ds_read_b64_tr_b16 v[74:75], v76
	ds_read_b64_tr_b16 v[76:77], v78
	s_add_i32 s16, 0, 0xa000
	v_add_u32_e32 v80, s16, v69
	ds_read_b64_tr_b16 v[78:79], v80
	v_readlane_b32 s16, v254, 61
	s_nop 1
	v_add_u32_e32 v82, s16, v69
	ds_read_b64_tr_b16 v[80:81], v82
	v_readlane_b32 s16, v254, 62
	s_nop 1
	v_add_u32_e32 v84, s16, v69
	ds_read_b64_tr_b16 v[82:83], v84
	v_readlane_b32 s16, v254, 63
	s_nop 1
	v_add_u32_e32 v86, s16, v69
	ds_read_b64_tr_b16 v[84:85], v86
	v_readlane_b32 s16, v255, 0
	s_nop 1
	v_add_u32_e32 v88, s16, v69
	ds_read_b64_tr_b16 v[86:87], v88
	v_readlane_b32 s16, v255, 1
	s_nop 1
	v_add_u32_e32 v90, s16, v69
	ds_read_b64_tr_b16 v[88:89], v90
	v_readlane_b32 s16, v255, 2
	s_nop 1
	v_add_u32_e32 v92, s16, v69
	ds_read_b64_tr_b16 v[90:91], v92
	v_readlane_b32 s16, v255, 3
	s_nop 1
	v_add_u32_e32 v95, s16, v69
	ds_read_b64_tr_b16 v[92:93], v95
	s_nop 0
	s_waitcnt lgkmcnt(0)
	s_or_b32 s15, s15, 0x3000
	v_mfma_f32_32x32x16_bf16 v[50:65], v[78:81], v[74:77], v[50:65]
	v_add_u32_e32 v71, s15, v71
	v_mfma_f32_32x32x16_bf16 v[34:49], v[82:85], v[74:77], v[34:49]
	v_mfma_f32_32x32x16_bf16 v[18:33], v[86:89], v[74:77], v[18:33]
	v_mfma_f32_32x32x16_bf16 v[2:17], v[90:93], v[74:77], v[2:17]
	ds_read_b64_tr_b16 v[74:75], v71
	v_add_u32_e32 v71, s15, v94
	ds_read_b64_tr_b16 v[76:77], v71
	s_add_i32 s15, 0, 0xb000
	v_add_u32_e32 v71, s15, v69
	ds_read_b64_tr_b16 v[78:79], v71
	v_readlane_b32 s15, v255, 4
	s_nop 1
	v_add_u32_e32 v71, s15, v69
	ds_read_b64_tr_b16 v[80:81], v71
	v_readlane_b32 s15, v255, 5
	s_nop 1
	v_add_u32_e32 v71, s15, v69
	ds_read_b64_tr_b16 v[82:83], v71
	v_readlane_b32 s15, v255, 6
	s_nop 1
	v_add_u32_e32 v71, s15, v69
	ds_read_b64_tr_b16 v[84:85], v71
	v_readlane_b32 s15, v255, 7
	s_nop 1
	v_add_u32_e32 v71, s15, v69
	ds_read_b64_tr_b16 v[86:87], v71
	v_readlane_b32 s15, v255, 8
	s_nop 1
	v_add_u32_e32 v71, s15, v69
	ds_read_b64_tr_b16 v[88:89], v71
	v_readlane_b32 s15, v255, 9
	s_nop 1
	v_add_u32_e32 v71, s15, v69
	ds_read_b64_tr_b16 v[90:91], v71
	v_readlane_b32 s15, v255, 10
	s_nop 1
	v_add_u32_e32 v69, s15, v69
	ds_read_b64_tr_b16 v[92:93], v69
	s_nop 0
	s_waitcnt lgkmcnt(0)
; __device__ __forceinline__ unsigned pk2(float lo, float hi) { return f2bf(lo) | (f2bf(hi) << 16); }
; __device__ __forceinline__ void gla_g1(LAS unsigned char* lds, const bf16* Z, bf16* ST, float* DEC, const GlaPre pre, const float (&wa)[16], const float ba, int item, int tid) {
;     ...
;     bf16* stp = ST + ((size_t)item * 256 + 32 * wid + r32) * 128 + 4 * hf;
; #pragma unroll
;     for (int kt = 0; kt < 4; ++kt)
; #pragma unroll
;         for (int g = 0; g < 4; ++g) { v2u w; w.x = pk2(acc[kt][4 * g], acc[kt][4 * g + 1]); w.y = pk2(acc[kt][4 * g + 2], acc[kt][4 * g + 3]); *(v2u*)(stp + 32 * kt + 8 * g) = w; }
	s_nop 0
	v_mfma_f32_32x32x16_bf16 v[50:65], v[78:81], v[74:77], v[50:65]
	s_lshl_b32 s14, s14, 5
	s_ashr_i32 s15, s14, 31
	s_add_u32 s14, s12, s14
	s_addc_u32 s15, s13, s15
	s_add_i32 s1, s1, s78
	v_mfma_f32_32x32x16_bf16 v[34:49], v[82:85], v[74:77], v[34:49]
	v_mfma_f32_32x32x16_bf16 v[18:33], v[86:89], v[74:77], v[18:33]
	v_mfma_f32_32x32x16_bf16 v[2:17], v[90:93], v[74:77], v[2:17]
	v_lshl_add_u64 v[74:75], s[14:15], 0, v[0:1]
	v_lshlrev_b64 v[74:75], 8, v[74:75]
	v_lshrrev_b32_e32 v0, 2, v70
	v_lshl_add_u64 v[74:75], s[4:5], 0, v[74:75]
	v_and_b32_e32 v0, 8, v0
	v_lshl_add_u64 v[70:71], v[74:75], 0, v[0:1]
	v_lshl_add_u64 v[74:75], v[0:1], 1, v[74:75]
	v_bfe_u32 v0, v50, 16, 1
	v_add3_u32 v0, v50, v0, s40
	v_bfe_u32 v50, v51, 16, 1
	v_lshrrev_b32_e32 v0, 16, v0
	v_add3_u32 v50, v51, v50, s40
	v_and_or_b32 v50, v50, s41, v0
	v_bfe_u32 v0, v52, 16, 1
	v_add3_u32 v0, v52, v0, s40
	v_bfe_u32 v51, v53, 16, 1
	v_lshrrev_b32_e32 v0, 16, v0
	v_add3_u32 v51, v53, v51, s40
	v_and_or_b32 v51, v51, s41, v0
	v_bfe_u32 v0, v54, 16, 1
	v_add3_u32 v0, v54, v0, s40
	v_bfe_u32 v52, v55, 16, 1
	v_lshrrev_b32_e32 v0, 16, v0
	v_add3_u32 v52, v55, v52, s40
	v_and_or_b32 v52, v52, s41, v0
	v_bfe_u32 v0, v56, 16, 1
	v_add3_u32 v0, v56, v0, s40
	v_bfe_u32 v53, v57, 16, 1
	v_lshrrev_b32_e32 v0, 16, v0
	v_add3_u32 v53, v57, v53, s40
	v_and_or_b32 v53, v53, s41, v0
	v_bfe_u32 v0, v58, 16, 1
	s_nop 0
	v_permlane32_swap_b32_e32 v50, v52
	v_permlane32_swap_b32_e32 v51, v53
	global_store_dwordx4 v[74:75], v[50:53], off offset:0
	s_nop 1
	v_add3_u32 v0, v58, v0, s40
	v_bfe_u32 v50, v59, 16, 1
	v_lshrrev_b32_e32 v0, 16, v0
	v_add3_u32 v50, v59, v50, s40
	v_and_or_b32 v50, v50, s41, v0
	v_bfe_u32 v0, v60, 16, 1
	v_add3_u32 v0, v60, v0, s40
	v_bfe_u32 v51, v61, 16, 1
	v_lshrrev_b32_e32 v0, 16, v0
	v_add3_u32 v51, v61, v51, s40
	v_and_or_b32 v51, v51, s41, v0
	v_bfe_u32 v0, v62, 16, 1
	v_add3_u32 v0, v62, v0, s40
	v_bfe_u32 v52, v63, 16, 1
	v_lshrrev_b32_e32 v0, 16, v0
	v_add3_u32 v52, v63, v52, s40
	v_and_or_b32 v52, v52, s41, v0
	v_bfe_u32 v0, v64, 16, 1
	v_add3_u32 v0, v64, v0, s40
	v_bfe_u32 v53, v65, 16, 1
	v_lshrrev_b32_e32 v0, 16, v0
	v_add3_u32 v53, v65, v53, s40
	v_and_or_b32 v53, v53, s41, v0
	v_bfe_u32 v0, v34, 16, 1
	v_add3_u32 v0, v34, v0, s40
	v_bfe_u32 v34, v35, 16, 1
	v_lshrrev_b32_e32 v0, 16, v0
	v_add3_u32 v34, v35, v34, s40
	v_and_or_b32 v34, v34, s41, v0
	v_bfe_u32 v0, v36, 16, 1
	v_add3_u32 v0, v36, v0, s40
	v_bfe_u32 v35, v37, 16, 1
	v_lshrrev_b32_e32 v0, 16, v0
	v_add3_u32 v35, v37, v35, s40
	v_and_or_b32 v35, v35, s41, v0
	v_bfe_u32 v0, v38, 16, 1
	v_add3_u32 v0, v38, v0, s40
	v_bfe_u32 v36, v39, 16, 1
	v_lshrrev_b32_e32 v0, 16, v0
	v_add3_u32 v36, v39, v36, s40
	v_and_or_b32 v36, v36, s41, v0
	v_bfe_u32 v0, v40, 16, 1
	v_add3_u32 v0, v40, v0, s40
	v_bfe_u32 v37, v41, 16, 1
	v_lshrrev_b32_e32 v0, 16, v0
	v_add3_u32 v37, v41, v37, s40
	v_and_or_b32 v37, v37, s41, v0
	v_bfe_u32 v0, v42, 16, 1
	s_nop 0
	v_permlane32_swap_b32_e32 v34, v36
	v_permlane32_swap_b32_e32 v35, v37
	global_store_dwordx4 v[74:75], v[34:37], off offset:64
	s_nop 1
	v_add3_u32 v0, v42, v0, s40
	v_bfe_u32 v34, v43, 16, 1
	v_lshrrev_b32_e32 v0, 16, v0
	v_add3_u32 v34, v43, v34, s40
	v_and_or_b32 v34, v34, s41, v0
	v_bfe_u32 v0, v44, 16, 1
	v_add3_u32 v0, v44, v0, s40
	v_bfe_u32 v35, v45, 16, 1
	v_lshrrev_b32_e32 v0, 16, v0
	v_add3_u32 v35, v45, v35, s40
	v_and_or_b32 v35, v35, s41, v0
	v_bfe_u32 v0, v46, 16, 1
	v_add3_u32 v0, v46, v0, s40
	v_bfe_u32 v36, v47, 16, 1
	v_lshrrev_b32_e32 v0, 16, v0
	v_add3_u32 v36, v47, v36, s40
	v_and_or_b32 v36, v36, s41, v0
	v_bfe_u32 v0, v48, 16, 1
	v_add3_u32 v0, v48, v0, s40
	v_bfe_u32 v37, v49, 16, 1
	v_lshrrev_b32_e32 v0, 16, v0
	v_add3_u32 v37, v49, v37, s40
	v_and_or_b32 v37, v37, s41, v0
	v_bfe_u32 v0, v18, 16, 1
	v_add3_u32 v0, v18, v0, s40
; __device__ __forceinline__ unsigned pk2(float lo, float hi) { return f2bf(lo) | (f2bf(hi) << 16); }
; __device__ __forceinline__ void gla_g1(LAS unsigned char* lds, const bf16* Z, bf16* ST, float* DEC, const GlaPre pre, const float (&wa)[16], const float ba, int item, int tid) {
;     ...
;     bf16* stp = ST + ((size_t)item * 256 + 32 * wid + r32) * 128 + 4 * hf;
; #pragma unroll
;     for (int kt = 0; kt < 4; ++kt)
; #pragma unroll
;         for (int g = 0; g < 4; ++g) { v2u w; w.x = pk2(acc[kt][4 * g], acc[kt][4 * g + 1]); w.y = pk2(acc[kt][4 * g + 2], acc[kt][4 * g + 3]); *(v2u*)(stp + 32 * kt + 8 * g) = w; }
;     __syncthreads();
	v_bfe_u32 v18, v19, 16, 1
	v_lshrrev_b32_e32 v0, 16, v0
	v_add3_u32 v18, v19, v18, s40
	v_and_or_b32 v18, v18, s41, v0
	v_bfe_u32 v0, v20, 16, 1
	v_add3_u32 v0, v20, v0, s40
	v_bfe_u32 v19, v21, 16, 1
	v_lshrrev_b32_e32 v0, 16, v0
	v_add3_u32 v19, v21, v19, s40
	v_and_or_b32 v19, v19, s41, v0
	v_bfe_u32 v0, v22, 16, 1
	v_add3_u32 v0, v22, v0, s40
	v_bfe_u32 v20, v23, 16, 1
	v_lshrrev_b32_e32 v0, 16, v0
	v_add3_u32 v20, v23, v20, s40
	v_and_or_b32 v20, v20, s41, v0
	v_bfe_u32 v0, v24, 16, 1
	v_add3_u32 v0, v24, v0, s40
	v_bfe_u32 v21, v25, 16, 1
	v_lshrrev_b32_e32 v0, 16, v0
	v_add3_u32 v21, v25, v21, s40
	v_and_or_b32 v21, v21, s41, v0
	v_bfe_u32 v0, v26, 16, 1
	s_nop 0
	v_permlane32_swap_b32_e32 v18, v20
	v_permlane32_swap_b32_e32 v19, v21
	global_store_dwordx4 v[74:75], v[18:21], off offset:128
	s_nop 1
	v_add3_u32 v0, v26, v0, s40
	v_bfe_u32 v18, v27, 16, 1
	v_lshrrev_b32_e32 v0, 16, v0
	v_add3_u32 v18, v27, v18, s40
	v_and_or_b32 v18, v18, s41, v0
	v_bfe_u32 v0, v28, 16, 1
	v_add3_u32 v0, v28, v0, s40
	v_bfe_u32 v19, v29, 16, 1
	v_lshrrev_b32_e32 v0, 16, v0
	v_add3_u32 v19, v29, v19, s40
	v_and_or_b32 v19, v19, s41, v0
	v_bfe_u32 v0, v30, 16, 1
	v_add3_u32 v0, v30, v0, s40
	v_bfe_u32 v20, v31, 16, 1
	v_lshrrev_b32_e32 v0, 16, v0
	v_add3_u32 v20, v31, v20, s40
	v_and_or_b32 v20, v20, s41, v0
	v_bfe_u32 v0, v32, 16, 1
	v_add3_u32 v0, v32, v0, s40
	v_bfe_u32 v21, v33, 16, 1
	v_lshrrev_b32_e32 v0, 16, v0
	v_add3_u32 v21, v33, v21, s40
	v_and_or_b32 v21, v21, s41, v0
	v_bfe_u32 v0, v2, 16, 1
	v_add3_u32 v0, v2, v0, s40
	v_bfe_u32 v2, v3, 16, 1
	v_lshrrev_b32_e32 v0, 16, v0
	v_add3_u32 v2, v3, v2, s40
	v_and_or_b32 v2, v2, s41, v0
	v_bfe_u32 v0, v4, 16, 1
	v_add3_u32 v0, v4, v0, s40
	v_bfe_u32 v3, v5, 16, 1
	v_lshrrev_b32_e32 v0, 16, v0
	v_add3_u32 v3, v5, v3, s40
	v_and_or_b32 v3, v3, s41, v0
	v_bfe_u32 v0, v6, 16, 1
	v_add3_u32 v0, v6, v0, s40
	v_bfe_u32 v4, v7, 16, 1
	v_lshrrev_b32_e32 v0, 16, v0
	v_add3_u32 v4, v7, v4, s40
	v_and_or_b32 v4, v4, s41, v0
	v_bfe_u32 v0, v8, 16, 1
	v_add3_u32 v0, v8, v0, s40
	v_bfe_u32 v5, v9, 16, 1
	v_lshrrev_b32_e32 v0, 16, v0
	v_add3_u32 v5, v9, v5, s40
	v_and_or_b32 v5, v5, s41, v0
	v_bfe_u32 v0, v10, 16, 1
	s_nop 0
	v_permlane32_swap_b32_e32 v2, v4
	v_permlane32_swap_b32_e32 v3, v5
	global_store_dwordx4 v[74:75], v[2:5], off offset:192
	s_nop 1
	v_add3_u32 v0, v10, v0, s40
	v_bfe_u32 v2, v11, 16, 1
	v_lshrrev_b32_e32 v0, 16, v0
	v_add3_u32 v2, v11, v2, s40
	v_and_or_b32 v2, v2, s41, v0
	v_bfe_u32 v0, v12, 16, 1
	v_add3_u32 v0, v12, v0, s40
	v_bfe_u32 v3, v13, 16, 1
	v_lshrrev_b32_e32 v0, 16, v0
	v_add3_u32 v3, v13, v3, s40
	v_and_or_b32 v3, v3, s41, v0
	v_bfe_u32 v0, v14, 16, 1
	v_readlane_b32 s14, v253, 59
	v_add3_u32 v0, v14, v0, s40
	v_bfe_u32 v4, v15, 16, 1
	s_add_i32 s0, s0, s14
	v_readlane_b32 s14, v254, 10
	v_lshrrev_b32_e32 v0, 16, v0
	v_add3_u32 v4, v15, v4, s40
	v_readlane_b32 s15, v254, 11
	s_add_u32 s12, s12, s14
	v_and_or_b32 v4, v4, s41, v0
	v_bfe_u32 v0, v16, 16, 1
	s_addc_u32 s13, s13, s15
	v_readlane_b32 s14, v255, 17
	v_add3_u32 v0, v16, v0, s40
	v_bfe_u32 v5, v17, 16, 1
	v_readlane_b32 s15, v255, 18
	s_add_u32 s10, s10, s14
	v_lshrrev_b32_e32 v0, 16, v0
	v_add3_u32 v5, v17, v5, s40
	s_addc_u32 s11, s11, s15
	v_and_or_b32 v5, v5, s41, v0
	s_cmpk_gt_i32 s1, 0x3ff
	s_nop 1
	v_permlane32_swap_b32_e32 v50, v52
	v_permlane32_swap_b32_e32 v51, v53
	global_store_dwordx4 v[74:75], v[50:53], off offset:32
	v_permlane32_swap_b32_e32 v34, v36
	v_permlane32_swap_b32_e32 v35, v37
	global_store_dwordx4 v[74:75], v[34:37], off offset:96
	v_permlane32_swap_b32_e32 v18, v20
	v_permlane32_swap_b32_e32 v19, v21
	global_store_dwordx4 v[74:75], v[18:21], off offset:160
	v_permlane32_swap_b32_e32 v2, v4
	v_permlane32_swap_b32_e32 v3, v5
	global_store_dwordx4 v[74:75], v[2:5], off offset:224
	s_barrier
	s_cbranch_scc1 .LBB0_924
